# grid barrier (in-layer copies): all waiters poll the top counter until it reaches (gen+1)*nx; generation-word updates and the waits on them dropped (two fewer dependent memory round trips per barrier)
# baseline (speedup 1.0000x reference)
; __device__ __forceinline__ unsigned xb_ld(unsigned* p)              { return __hip_atomic_load(p, __ATOMIC_RELAXED, __HIP_MEMORY_SCOPE_AGENT); }
; __device__ __forceinline__ unsigned xb_add(unsigned* p, unsigned v) { return __hip_atomic_fetch_add(p, v, __ATOMIC_RELAXED, __HIP_MEMORY_SCOPE_AGENT); }
; #define XB_SPIN(cond, bar) do { unsigned _sp = 0; while (cond) { __builtin_amdgcn_s_sleep(1); \
;     if ((++_sp & 255u) == 0u) { if (xb_ld(&(bar)[XB_TMO])) break; if (_sp > XB_SPIN_CAP) { atomicAdd(&(bar)[XB_TMO], 1u); break; } } } } while (0)
; __device__ __forceinline__ void xcd_barrier(const XcdBarrier& b) {
;     ...
;             __builtin_amdgcn_fence(__ATOMIC_RELEASE, "agent");
;             asm volatile("s_waitcnt vmcnt(0)" ::: "memory");
;             const unsigned og = xb_add(&bar[XB_TOP], 1u);
;             const unsigned tg = og / nx;
;             if (og + 1u == (tg + 1u) * nx) xb_add(&bar[XB_TOPGEN], 1u);
;             else XB_SPIN(xb_ld(&bar[XB_TOPGEN]) == tg, bar);
;             __builtin_amdgcn_fence(__ATOMIC_ACQUIRE, "agent");
;             xb_add(&bar[XB_XGEN(b.x)], 1u);
;             asm volatile("s_waitcnt vmcnt(0)" ::: "memory");
.LBB0_262:
	s_or_b64 exec, exec, s[18:19]
	s_waitcnt vmcnt(0)
	buffer_inv sc1
	s_waitcnt vmcnt(0)

; __device__ __forceinline__ unsigned xb_ld(unsigned* p)              { return __hip_atomic_load(p, __ATOMIC_RELAXED, __HIP_MEMORY_SCOPE_AGENT); }
; __device__ __forceinline__ unsigned xb_add(unsigned* p, unsigned v) { return __hip_atomic_fetch_add(p, v, __ATOMIC_RELAXED, __HIP_MEMORY_SCOPE_AGENT); }
; #define XB_SPIN(cond, bar) do { unsigned _sp = 0; while (cond) { __builtin_amdgcn_s_sleep(1); \
;     if ((++_sp & 255u) == 0u) { if (xb_ld(&(bar)[XB_TMO])) break; if (_sp > XB_SPIN_CAP) { atomicAdd(&(bar)[XB_TMO], 1u); break; } } } } while (0)
; __device__ __forceinline__ void xcd_barrier(const XcdBarrier& b) {
;     ...
;         const unsigned old = xb_add(&bar[XB_XSUB(b.x)], 1u);
;         const unsigned gen = old / nloc;
;         if (old + 1u == (gen + 1u) * nloc) {
;             __builtin_amdgcn_fence(__ATOMIC_RELEASE, "agent");
;             asm volatile("s_waitcnt vmcnt(0)" ::: "memory");
;             const unsigned og = xb_add(&bar[XB_TOP], 1u);
;             const unsigned tg = og / nx;
;             if (og + 1u == (tg + 1u) * nx) xb_add(&bar[XB_TOPGEN], 1u);
;             else XB_SPIN(xb_ld(&bar[XB_TOPGEN]) == tg, bar);
;             __builtin_amdgcn_fence(__ATOMIC_ACQUIRE, "agent");
;             xb_add(&bar[XB_XGEN(b.x)], 1u);
;             asm volatile("s_waitcnt vmcnt(0)" ::: "memory");
;         } else {
;             XB_SPIN(xb_ld(&bar[XB_XGEN(b.x)]) == gen, bar);
.LBB0_348:
	v_readlane_b32 s8, v254, 8
	v_readlane_b32 s9, v254, 9
	v_cvt_f32_u32_e32 v1, v2
	v_sub_u32_e32 v4, 0, v2
	v_rcp_iflag_f32_e32 v1, v1
	s_nop 1
	global_atomic_add v3, v193, v226, s[8:9] sc0
	v_mul_f32_e32 v1, 0x4f7ffffe, v1
	v_cvt_u32_f32_e32 v1, v1
	v_mul_lo_u32 v4, v4, v1
	v_mul_hi_u32 v4, v1, v4
	v_add_u32_e32 v1, v1, v4
	s_waitcnt vmcnt(0)
	v_mul_hi_u32 v1, v3, v1
	v_mul_lo_u32 v4, v1, v2
	v_sub_u32_e32 v4, v3, v4
	v_add_u32_e32 v5, 1, v1
	v_cmp_ge_u32_e32 vcc, v4, v2
	v_add_u32_e32 v3, 1, v3
	s_nop 0
	v_cndmask_b32_e32 v1, v1, v5, vcc
	v_sub_u32_e32 v5, v4, v2
	v_cndmask_b32_e32 v4, v4, v5, vcc
	v_add_u32_e32 v5, 1, v1
	v_cmp_ge_u32_e32 vcc, v4, v2
	s_nop 1
	v_cndmask_b32_e32 v1, v1, v5, vcc
	v_mul_lo_u32 v4, v2, v1
	v_add_u32_e32 v2, v4, v2
	v_cmp_ne_u32_e32 vcc, v3, v2
	s_and_saveexec_b64 s[18:19], vcc
	s_xor_b64 s[36:37], exec, s[18:19]
	s_cbranch_execz .LBB0_362
	v_readlane_b32 s8, v254, 12
	v_readlane_b32 s9, v254, 13
	s_waitcnt lgkmcnt(0)
	v_add_u32_e32 v5, 1, v1
	v_mul_lo_u32 v5, v5, v0
	s_nop 3
	global_load_dword v0, v193, s[8:9] sc1
	s_waitcnt vmcnt(0)
	v_cmp_lt_u32_e32 vcc, v0, v5
	s_and_saveexec_b64 s[38:39], vcc
	s_cbranch_execz .LBB0_361
	s_mov_b32 s5, 1
	s_mov_b64 s[40:41], 0
	s_branch .LBB0_352

; __device__ __forceinline__ unsigned xb_ld(unsigned* p)              { return __hip_atomic_load(p, __ATOMIC_RELAXED, __HIP_MEMORY_SCOPE_AGENT); }
; #define XB_SPIN(cond, bar) do { unsigned _sp = 0; while (cond) { __builtin_amdgcn_s_sleep(1); \
;     if ((++_sp & 255u) == 0u) { if (xb_ld(&(bar)[XB_TMO])) break; if (_sp > XB_SPIN_CAP) { atomicAdd(&(bar)[XB_TMO], 1u); break; } } } } while (0)
; __device__ __forceinline__ void xcd_barrier(const XcdBarrier& b) {
;     ...
;             XB_SPIN(xb_ld(&bar[XB_XGEN(b.x)]) == gen, bar);
.LBB0_356:
	v_readlane_b32 s8, v254, 12
	v_readlane_b32 s9, v254, 13
	s_add_i32 s5, s5, 1
	s_mov_b64 s[46:47], -1
	s_nop 2
	global_load_dword v0, v193, s[8:9] sc1
	s_waitcnt vmcnt(0)
	v_cmp_ge_u32_e32 vcc, v0, v5
	s_orn2_b64 s[44:45], vcc, exec
	s_branch .LBB0_351

; __device__ __forceinline__ unsigned xb_ld(unsigned* p)              { return __hip_atomic_load(p, __ATOMIC_RELAXED, __HIP_MEMORY_SCOPE_AGENT); }
; __device__ __forceinline__ unsigned xb_add(unsigned* p, unsigned v) { return __hip_atomic_fetch_add(p, v, __ATOMIC_RELAXED, __HIP_MEMORY_SCOPE_AGENT); }
; #define XB_SPIN(cond, bar) do { unsigned _sp = 0; while (cond) { __builtin_amdgcn_s_sleep(1); \
;     if ((++_sp & 255u) == 0u) { if (xb_ld(&(bar)[XB_TMO])) break; if (_sp > XB_SPIN_CAP) { atomicAdd(&(bar)[XB_TMO], 1u); break; } } } } while (0)
; __device__ __forceinline__ void xcd_barrier(const XcdBarrier& b) {
;     ...
;             const unsigned og = xb_add(&bar[XB_TOP], 1u);
;             const unsigned tg = og / nx;
;             if (og + 1u == (tg + 1u) * nx) xb_add(&bar[XB_TOPGEN], 1u);
;             else XB_SPIN(xb_ld(&bar[XB_TOPGEN]) == tg, bar);
.LBB0_365:
	s_or_b64 exec, exec, s[38:39]
	s_waitcnt vmcnt(0)
	v_readfirstlane_b32 s0, v2
	v_cvt_f32_u32_e32 v2, v0
	v_sub_u32_e32 v3, 0, v0
	v_add_u32_e32 v1, s0, v1
	v_readlane_b32 s8, v254, 14
	v_rcp_iflag_f32_e32 v2, v2
	v_readlane_b32 s9, v254, 15
	s_mov_b64 s[38:39], -1
	v_mul_f32_e32 v2, 0x4f7ffffe, v2
	v_cvt_u32_f32_e32 v2, v2
	v_mul_lo_u32 v3, v3, v2
	v_mul_hi_u32 v3, v2, v3
	v_add_u32_e32 v2, v2, v3
	v_mul_hi_u32 v2, v1, v2
	v_mul_lo_u32 v3, v2, v0
	v_sub_u32_e32 v3, v1, v3
	v_cmp_ge_u32_e32 vcc, v3, v0
	v_add_u32_e32 v4, 1, v2
	v_add_u32_e32 v1, 1, v1
	v_cndmask_b32_e32 v2, v2, v4, vcc
	v_sub_u32_e32 v4, v3, v0
	v_cndmask_b32_e32 v3, v3, v4, vcc
	v_cmp_ge_u32_e32 vcc, v3, v0
	v_add_u32_e32 v3, 1, v2
	s_nop 0
	v_cndmask_b32_e32 v2, v2, v3, vcc
	v_mul_lo_u32 v3, v0, v2
	v_add_u32_e32 v0, v3, v0
	v_cmp_ne_u32_e32 vcc, v1, v0
	v_mov_b32_e32 v5, v0
	v_mov_b64_e32 v[0:1], s[8:9]
	s_and_saveexec_b64 s[36:37], vcc
	s_cbranch_execz .LBB0_377
	v_readlane_b32 s8, v254, 12
	v_readlane_b32 s9, v254, 13
	s_mov_b64 s[40:41], 0
	s_nop 3
	global_load_dword v0, v193, s[8:9] sc1
	s_waitcnt vmcnt(0)
	v_cmp_lt_u32_e32 vcc, v0, v5
	s_and_saveexec_b64 s[38:39], vcc
	s_cbranch_execz .LBB0_376
	s_mov_b32 s5, 1
	s_branch .LBB0_369

; __device__ __forceinline__ unsigned xb_ld(unsigned* p)              { return __hip_atomic_load(p, __ATOMIC_RELAXED, __HIP_MEMORY_SCOPE_AGENT); }
; __device__ __forceinline__ unsigned xb_add(unsigned* p, unsigned v) { return __hip_atomic_fetch_add(p, v, __ATOMIC_RELAXED, __HIP_MEMORY_SCOPE_AGENT); }
; #define XB_SPIN(cond, bar) do { unsigned _sp = 0; while (cond) { __builtin_amdgcn_s_sleep(1); \
;     if ((++_sp & 255u) == 0u) { if (xb_ld(&(bar)[XB_TMO])) break; if (_sp > XB_SPIN_CAP) { atomicAdd(&(bar)[XB_TMO], 1u); break; } } } } while (0)
; __device__ __forceinline__ void xcd_barrier(const XcdBarrier& b) {
;     ...
;             if (og + 1u == (tg + 1u) * nx) xb_add(&bar[XB_TOPGEN], 1u);
;             else XB_SPIN(xb_ld(&bar[XB_TOPGEN]) == tg, bar);
;             __builtin_amdgcn_fence(__ATOMIC_ACQUIRE, "agent");
;             xb_add(&bar[XB_XGEN(b.x)], 1u);
;             asm volatile("s_waitcnt vmcnt(0)" ::: "memory");
.LBB0_377:
	s_or_b64 exec, exec, s[36:37]
	s_and_saveexec_b64 s[36:37], s[38:39]
	s_cbranch_execz .LBB0_379
.LBB0_379:
	s_or_b64 exec, exec, s[36:37]
	s_waitcnt vmcnt(0)
	buffer_inv sc1
	s_waitcnt vmcnt(0)
.LBB0_380:
	s_or_b64 exec, exec, s[2:3]
	s_waitcnt lgkmcnt(0)
	s_barrier

; __device__ __forceinline__ unsigned xb_ld(unsigned* p)              { return __hip_atomic_load(p, __ATOMIC_RELAXED, __HIP_MEMORY_SCOPE_AGENT); }
; __device__ __forceinline__ unsigned xb_add(unsigned* p, unsigned v) { return __hip_atomic_fetch_add(p, v, __ATOMIC_RELAXED, __HIP_MEMORY_SCOPE_AGENT); }
; #define XB_SPIN(cond, bar) do { unsigned _sp = 0; while (cond) { __builtin_amdgcn_s_sleep(1); \
;     if ((++_sp & 255u) == 0u) { if (xb_ld(&(bar)[XB_TMO])) break; if (_sp > XB_SPIN_CAP) { atomicAdd(&(bar)[XB_TMO], 1u); break; } } } } while (0)
; __device__ __forceinline__ void xcd_barrier(const XcdBarrier& b) {
;     ...
;             if (og + 1u == (tg + 1u) * nx) xb_add(&bar[XB_TOPGEN], 1u);
;             else XB_SPIN(xb_ld(&bar[XB_TOPGEN]) == tg, bar);
;             __builtin_amdgcn_fence(__ATOMIC_ACQUIRE, "agent");
;             xb_add(&bar[XB_XGEN(b.x)], 1u);
;             asm volatile("s_waitcnt vmcnt(0)" ::: "memory");
.LBB0_465:
	s_or_b64 exec, exec, s[36:37]
	s_and_saveexec_b64 s[36:37], s[38:39]
	s_cbranch_execz .LBB0_467
.LBB0_467:
	s_or_b64 exec, exec, s[36:37]
	s_waitcnt vmcnt(0)
	buffer_inv sc1
	s_waitcnt vmcnt(0)
.LBB0_468:
	s_or_b64 exec, exec, s[2:3]
	s_waitcnt lgkmcnt(0)
	s_barrier

; __device__ __forceinline__ unsigned xb_ld(unsigned* p)              { return __hip_atomic_load(p, __ATOMIC_RELAXED, __HIP_MEMORY_SCOPE_AGENT); }
; __device__ __forceinline__ unsigned xb_add(unsigned* p, unsigned v) { return __hip_atomic_fetch_add(p, v, __ATOMIC_RELAXED, __HIP_MEMORY_SCOPE_AGENT); }
; #define XB_SPIN(cond, bar) do { unsigned _sp = 0; while (cond) { __builtin_amdgcn_s_sleep(1); \
;     if ((++_sp & 255u) == 0u) { if (xb_ld(&(bar)[XB_TMO])) break; if (_sp > XB_SPIN_CAP) { atomicAdd(&(bar)[XB_TMO], 1u); break; } } } } while (0)
; __device__ __forceinline__ void xcd_barrier(const XcdBarrier& b) {
;     ...
;             if (og + 1u == (tg + 1u) * nx) xb_add(&bar[XB_TOPGEN], 1u);
;             else XB_SPIN(xb_ld(&bar[XB_TOPGEN]) == tg, bar);
;             __builtin_amdgcn_fence(__ATOMIC_ACQUIRE, "agent");
;             xb_add(&bar[XB_XGEN(b.x)], 1u);
;             asm volatile("s_waitcnt vmcnt(0)" ::: "memory");
.LBB0_596:
	s_or_b64 exec, exec, s[36:37]
	s_and_saveexec_b64 s[36:37], s[38:39]
	s_cbranch_execz .LBB0_598
.LBB0_598:
	s_or_b64 exec, exec, s[36:37]
	s_waitcnt vmcnt(0)
	buffer_inv sc1
	s_waitcnt vmcnt(0)
.LBB0_599:
	s_or_b64 exec, exec, s[2:3]
	s_waitcnt lgkmcnt(0)
	s_barrier

; __device__ __forceinline__ unsigned xb_ld(unsigned* p)              { return __hip_atomic_load(p, __ATOMIC_RELAXED, __HIP_MEMORY_SCOPE_AGENT); }
; __device__ __forceinline__ unsigned xb_add(unsigned* p, unsigned v) { return __hip_atomic_fetch_add(p, v, __ATOMIC_RELAXED, __HIP_MEMORY_SCOPE_AGENT); }
; #define XB_SPIN(cond, bar) do { unsigned _sp = 0; while (cond) { __builtin_amdgcn_s_sleep(1); \
;     if ((++_sp & 255u) == 0u) { if (xb_ld(&(bar)[XB_TMO])) break; if (_sp > XB_SPIN_CAP) { atomicAdd(&(bar)[XB_TMO], 1u); break; } } } } while (0)
; __device__ __forceinline__ void xcd_barrier(const XcdBarrier& b) {
;     ...
;             if (og + 1u == (tg + 1u) * nx) xb_add(&bar[XB_TOPGEN], 1u);
;             else XB_SPIN(xb_ld(&bar[XB_TOPGEN]) == tg, bar);
;             __builtin_amdgcn_fence(__ATOMIC_ACQUIRE, "agent");
;             xb_add(&bar[XB_XGEN(b.x)], 1u);
;             asm volatile("s_waitcnt vmcnt(0)" ::: "memory");
.LBB0_681:
	s_or_b64 exec, exec, s[36:37]
	s_and_saveexec_b64 s[36:37], s[38:39]
	s_cbranch_execz .LBB0_683
.LBB0_683:
	s_or_b64 exec, exec, s[36:37]
	s_waitcnt vmcnt(0)
	buffer_inv sc1
	s_waitcnt vmcnt(0)
.LBB0_684:
	s_or_b64 exec, exec, s[2:3]
	s_waitcnt lgkmcnt(0)
	s_barrier

; __device__ __forceinline__ unsigned xb_ld(unsigned* p)              { return __hip_atomic_load(p, __ATOMIC_RELAXED, __HIP_MEMORY_SCOPE_AGENT); }
; __device__ __forceinline__ unsigned xb_add(unsigned* p, unsigned v) { return __hip_atomic_fetch_add(p, v, __ATOMIC_RELAXED, __HIP_MEMORY_SCOPE_AGENT); }
; #define XB_SPIN(cond, bar) do { unsigned _sp = 0; while (cond) { __builtin_amdgcn_s_sleep(1); \
;     if ((++_sp & 255u) == 0u) { if (xb_ld(&(bar)[XB_TMO])) break; if (_sp > XB_SPIN_CAP) { atomicAdd(&(bar)[XB_TMO], 1u); break; } } } } while (0)
; __device__ __forceinline__ void xcd_barrier(const XcdBarrier& b) {
;     ...
;             if (og + 1u == (tg + 1u) * nx) xb_add(&bar[XB_TOPGEN], 1u);
;             else XB_SPIN(xb_ld(&bar[XB_TOPGEN]) == tg, bar);
;             __builtin_amdgcn_fence(__ATOMIC_ACQUIRE, "agent");
;             xb_add(&bar[XB_XGEN(b.x)], 1u);
;             asm volatile("s_waitcnt vmcnt(0)" ::: "memory");
.LBB0_766:
	s_or_b64 exec, exec, s[36:37]
	s_and_saveexec_b64 s[36:37], s[38:39]
	s_cbranch_execz .LBB0_768
.LBB0_768:
	s_or_b64 exec, exec, s[36:37]
	s_waitcnt vmcnt(0)
	buffer_inv sc1
	s_waitcnt vmcnt(0)
.LBB0_769:
	s_or_b64 exec, exec, s[2:3]
	s_waitcnt lgkmcnt(0)
	s_barrier

; __device__ __forceinline__ unsigned xb_ld(unsigned* p)              { return __hip_atomic_load(p, __ATOMIC_RELAXED, __HIP_MEMORY_SCOPE_AGENT); }
; __device__ __forceinline__ unsigned xb_add(unsigned* p, unsigned v) { return __hip_atomic_fetch_add(p, v, __ATOMIC_RELAXED, __HIP_MEMORY_SCOPE_AGENT); }
; #define XB_SPIN(cond, bar) do { unsigned _sp = 0; while (cond) { __builtin_amdgcn_s_sleep(1); \
;     if ((++_sp & 255u) == 0u) { if (xb_ld(&(bar)[XB_TMO])) break; if (_sp > XB_SPIN_CAP) { atomicAdd(&(bar)[XB_TMO], 1u); break; } } } } while (0)
; __device__ __forceinline__ void xcd_barrier(const XcdBarrier& b) {
;     ...
;             if (og + 1u == (tg + 1u) * nx) xb_add(&bar[XB_TOPGEN], 1u);
;             else XB_SPIN(xb_ld(&bar[XB_TOPGEN]) == tg, bar);
;             __builtin_amdgcn_fence(__ATOMIC_ACQUIRE, "agent");
;             xb_add(&bar[XB_XGEN(b.x)], 1u);
;             asm volatile("s_waitcnt vmcnt(0)" ::: "memory");
.LBB0_822:
	s_or_b64 exec, exec, s[36:37]
	s_and_saveexec_b64 s[36:37], s[38:39]
	s_cbranch_execz .LBB0_824
.LBB0_824:
	s_or_b64 exec, exec, s[36:37]
	s_waitcnt vmcnt(0)
	buffer_inv sc1
	s_waitcnt vmcnt(0)
.LBB0_825:
	s_or_b64 exec, exec, s[2:3]
	s_waitcnt lgkmcnt(0)
	s_barrier

; __device__ __forceinline__ unsigned xb_ld(unsigned* p)              { return __hip_atomic_load(p, __ATOMIC_RELAXED, __HIP_MEMORY_SCOPE_AGENT); }
; __device__ __forceinline__ unsigned xb_add(unsigned* p, unsigned v) { return __hip_atomic_fetch_add(p, v, __ATOMIC_RELAXED, __HIP_MEMORY_SCOPE_AGENT); }
; #define XB_SPIN(cond, bar) do { unsigned _sp = 0; while (cond) { __builtin_amdgcn_s_sleep(1); \
;     if ((++_sp & 255u) == 0u) { if (xb_ld(&(bar)[XB_TMO])) break; if (_sp > XB_SPIN_CAP) { atomicAdd(&(bar)[XB_TMO], 1u); break; } } } } while (0)
; __device__ __forceinline__ void xcd_barrier(const XcdBarrier& b) {
;     ...
;         const unsigned old = xb_add(&bar[XB_XSUB(b.x)], 1u);
;         const unsigned gen = old / nloc;
;         if (old + 1u == (gen + 1u) * nloc) {
;             __builtin_amdgcn_fence(__ATOMIC_RELEASE, "agent");
;             asm volatile("s_waitcnt vmcnt(0)" ::: "memory");
;             const unsigned og = xb_add(&bar[XB_TOP], 1u);
;             const unsigned tg = og / nx;
;             if (og + 1u == (tg + 1u) * nx) xb_add(&bar[XB_TOPGEN], 1u);
;             else XB_SPIN(xb_ld(&bar[XB_TOPGEN]) == tg, bar);
;             __builtin_amdgcn_fence(__ATOMIC_ACQUIRE, "agent");
;             xb_add(&bar[XB_XGEN(b.x)], 1u);
;             asm volatile("s_waitcnt vmcnt(0)" ::: "memory");
;         } else {
;             XB_SPIN(xb_ld(&bar[XB_XGEN(b.x)]) == gen, bar);
.LBB0_878:
	v_readlane_b32 s8, v254, 8
	v_readlane_b32 s9, v254, 9
	v_cvt_f32_u32_e32 v1, v2
	v_sub_u32_e32 v4, 0, v2
	v_rcp_iflag_f32_e32 v1, v1
	s_nop 1
	global_atomic_add v3, v193, v226, s[8:9] sc0
	v_mul_f32_e32 v1, 0x4f7ffffe, v1
	v_cvt_u32_f32_e32 v1, v1
	v_mul_lo_u32 v4, v4, v1
	v_mul_hi_u32 v4, v1, v4
	v_add_u32_e32 v1, v1, v4
	s_waitcnt vmcnt(0)
	v_mul_hi_u32 v1, v3, v1
	v_mul_lo_u32 v4, v1, v2
	v_sub_u32_e32 v4, v3, v4
	v_add_u32_e32 v5, 1, v1
	v_cmp_ge_u32_e32 vcc, v4, v2
	v_add_u32_e32 v3, 1, v3
	s_nop 0
	v_cndmask_b32_e32 v1, v1, v5, vcc
	v_sub_u32_e32 v5, v4, v2
	v_cndmask_b32_e32 v4, v4, v5, vcc
	v_add_u32_e32 v5, 1, v1
	v_cmp_ge_u32_e32 vcc, v4, v2
	s_nop 1
	v_cndmask_b32_e32 v1, v1, v5, vcc
	v_mul_lo_u32 v4, v2, v1
	v_add_u32_e32 v2, v4, v2
	v_cmp_ne_u32_e32 vcc, v3, v2
	s_and_saveexec_b64 s[18:19], vcc
	s_xor_b64 s[20:21], exec, s[18:19]
	s_cbranch_execz .LBB0_892
	v_readlane_b32 s8, v254, 12
	v_readlane_b32 s9, v254, 13
	s_waitcnt lgkmcnt(0)
	v_add_u32_e32 v5, 1, v1
	v_mul_lo_u32 v5, v5, v0
	s_nop 3
	global_load_dword v0, v193, s[8:9] sc1
	s_waitcnt vmcnt(0)
	v_cmp_lt_u32_e32 vcc, v0, v5
	s_and_saveexec_b64 s[36:37], vcc
	s_cbranch_execz .LBB0_891
	s_mov_b32 s5, 1
	s_mov_b64 s[38:39], 0
	s_branch .LBB0_882

; __device__ __forceinline__ unsigned xb_ld(unsigned* p)              { return __hip_atomic_load(p, __ATOMIC_RELAXED, __HIP_MEMORY_SCOPE_AGENT); }
; #define XB_SPIN(cond, bar) do { unsigned _sp = 0; while (cond) { __builtin_amdgcn_s_sleep(1); \
;     if ((++_sp & 255u) == 0u) { if (xb_ld(&(bar)[XB_TMO])) break; if (_sp > XB_SPIN_CAP) { atomicAdd(&(bar)[XB_TMO], 1u); break; } } } } while (0)
; __device__ __forceinline__ void xcd_barrier(const XcdBarrier& b) {
;     ...
;             XB_SPIN(xb_ld(&bar[XB_XGEN(b.x)]) == gen, bar);
.LBB0_886:
	v_readlane_b32 s8, v254, 12
	v_readlane_b32 s9, v254, 13
	s_add_i32 s5, s5, 1
	s_mov_b64 s[44:45], -1
	s_nop 2
	global_load_dword v0, v193, s[8:9] sc1
	s_waitcnt vmcnt(0)
	v_cmp_ge_u32_e32 vcc, v0, v5
	s_orn2_b64 s[42:43], vcc, exec
	s_branch .LBB0_881

; __device__ __forceinline__ unsigned xb_ld(unsigned* p)              { return __hip_atomic_load(p, __ATOMIC_RELAXED, __HIP_MEMORY_SCOPE_AGENT); }
; __device__ __forceinline__ unsigned xb_add(unsigned* p, unsigned v) { return __hip_atomic_fetch_add(p, v, __ATOMIC_RELAXED, __HIP_MEMORY_SCOPE_AGENT); }
; #define XB_SPIN(cond, bar) do { unsigned _sp = 0; while (cond) { __builtin_amdgcn_s_sleep(1); \
;     if ((++_sp & 255u) == 0u) { if (xb_ld(&(bar)[XB_TMO])) break; if (_sp > XB_SPIN_CAP) { atomicAdd(&(bar)[XB_TMO], 1u); break; } } } } while (0)
; __device__ __forceinline__ void xcd_barrier(const XcdBarrier& b) {
;     ...
;             const unsigned og = xb_add(&bar[XB_TOP], 1u);
;             const unsigned tg = og / nx;
;             if (og + 1u == (tg + 1u) * nx) xb_add(&bar[XB_TOPGEN], 1u);
;             else XB_SPIN(xb_ld(&bar[XB_TOPGEN]) == tg, bar);
.LBB0_895:
	s_or_b64 exec, exec, s[36:37]
	s_waitcnt vmcnt(0)
	v_readfirstlane_b32 s0, v2
	v_cvt_f32_u32_e32 v2, v0
	v_sub_u32_e32 v3, 0, v0
	v_add_u32_e32 v1, s0, v1
	v_readlane_b32 s8, v254, 14
	v_rcp_iflag_f32_e32 v2, v2
	v_readlane_b32 s9, v254, 15
	s_mov_b64 s[36:37], -1
	v_mul_f32_e32 v2, 0x4f7ffffe, v2
	v_cvt_u32_f32_e32 v2, v2
	v_mul_lo_u32 v3, v3, v2
	v_mul_hi_u32 v3, v2, v3
	v_add_u32_e32 v2, v2, v3
	v_mul_hi_u32 v2, v1, v2
	v_mul_lo_u32 v3, v2, v0
	v_sub_u32_e32 v3, v1, v3
	v_cmp_ge_u32_e32 vcc, v3, v0
	v_add_u32_e32 v4, 1, v2
	v_add_u32_e32 v1, 1, v1
	v_cndmask_b32_e32 v2, v2, v4, vcc
	v_sub_u32_e32 v4, v3, v0
	v_cndmask_b32_e32 v3, v3, v4, vcc
	v_cmp_ge_u32_e32 vcc, v3, v0
	v_add_u32_e32 v3, 1, v2
	s_nop 0
	v_cndmask_b32_e32 v2, v2, v3, vcc
	v_mul_lo_u32 v3, v0, v2
	v_add_u32_e32 v0, v3, v0
	v_cmp_ne_u32_e32 vcc, v1, v0
	v_mov_b32_e32 v5, v0
	v_mov_b64_e32 v[0:1], s[8:9]
	s_and_saveexec_b64 s[20:21], vcc
	s_cbranch_execz .LBB0_907
	v_readlane_b32 s8, v254, 12
	v_readlane_b32 s9, v254, 13
	s_mov_b64 s[38:39], 0
	s_nop 3
	global_load_dword v0, v193, s[8:9] sc1
	s_waitcnt vmcnt(0)
	v_cmp_lt_u32_e32 vcc, v0, v5
	s_and_saveexec_b64 s[36:37], vcc
	s_cbranch_execz .LBB0_906
	s_mov_b32 s5, 1
	s_branch .LBB0_899

; __device__ __forceinline__ unsigned xb_ld(unsigned* p)              { return __hip_atomic_load(p, __ATOMIC_RELAXED, __HIP_MEMORY_SCOPE_AGENT); }
; __device__ __forceinline__ unsigned xb_add(unsigned* p, unsigned v) { return __hip_atomic_fetch_add(p, v, __ATOMIC_RELAXED, __HIP_MEMORY_SCOPE_AGENT); }
; #define XB_SPIN(cond, bar) do { unsigned _sp = 0; while (cond) { __builtin_amdgcn_s_sleep(1); \
;     if ((++_sp & 255u) == 0u) { if (xb_ld(&(bar)[XB_TMO])) break; if (_sp > XB_SPIN_CAP) { atomicAdd(&(bar)[XB_TMO], 1u); break; } } } } while (0)
; __device__ __forceinline__ void xcd_barrier(const XcdBarrier& b) {
;     ...
;             if (og + 1u == (tg + 1u) * nx) xb_add(&bar[XB_TOPGEN], 1u);
;             else XB_SPIN(xb_ld(&bar[XB_TOPGEN]) == tg, bar);
;             __builtin_amdgcn_fence(__ATOMIC_ACQUIRE, "agent");
;             xb_add(&bar[XB_XGEN(b.x)], 1u);
;             asm volatile("s_waitcnt vmcnt(0)" ::: "memory");
.LBB0_907:
	s_or_b64 exec, exec, s[20:21]
	s_and_saveexec_b64 s[20:21], s[36:37]
	s_cbranch_execz .LBB0_909
.LBB0_909:
	s_or_b64 exec, exec, s[20:21]
	s_waitcnt vmcnt(0)
	buffer_inv sc1
	s_waitcnt vmcnt(0)
.LBB0_910:
	s_or_b64 exec, exec, s[2:3]
	s_waitcnt lgkmcnt(0)
	s_barrier

; __device__ __forceinline__ unsigned xb_ld(unsigned* p)              { return __hip_atomic_load(p, __ATOMIC_RELAXED, __HIP_MEMORY_SCOPE_AGENT); }
; __device__ __forceinline__ unsigned xb_add(unsigned* p, unsigned v) { return __hip_atomic_fetch_add(p, v, __ATOMIC_RELAXED, __HIP_MEMORY_SCOPE_AGENT); }
; #define XB_SPIN(cond, bar) do { unsigned _sp = 0; while (cond) { __builtin_amdgcn_s_sleep(1); \
;     if ((++_sp & 255u) == 0u) { if (xb_ld(&(bar)[XB_TMO])) break; if (_sp > XB_SPIN_CAP) { atomicAdd(&(bar)[XB_TMO], 1u); break; } } } } while (0)
; __device__ __forceinline__ void xcd_barrier(const XcdBarrier& b) {
;     ...
;             if (og + 1u == (tg + 1u) * nx) xb_add(&bar[XB_TOPGEN], 1u);
;             else XB_SPIN(xb_ld(&bar[XB_TOPGEN]) == tg, bar);
;             __builtin_amdgcn_fence(__ATOMIC_ACQUIRE, "agent");
;             xb_add(&bar[XB_XGEN(b.x)], 1u);
;             asm volatile("s_waitcnt vmcnt(0)" ::: "memory");
.LBB0_1344:
	s_or_b64 exec, exec, s[20:21]
	s_and_saveexec_b64 s[20:21], s[36:37]
	s_cbranch_execz .LBB0_1346
.LBB0_1346:
	s_or_b64 exec, exec, s[20:21]
	s_waitcnt vmcnt(0)
	buffer_inv sc1
	s_waitcnt vmcnt(0)
.LBB0_1347:
	s_or_b64 exec, exec, s[2:3]
	s_waitcnt lgkmcnt(0)
	s_barrier

; __device__ __forceinline__ unsigned xb_ld(unsigned* p)              { return __hip_atomic_load(p, __ATOMIC_RELAXED, __HIP_MEMORY_SCOPE_AGENT); }
; __device__ __forceinline__ unsigned xb_add(unsigned* p, unsigned v) { return __hip_atomic_fetch_add(p, v, __ATOMIC_RELAXED, __HIP_MEMORY_SCOPE_AGENT); }
; #define XB_SPIN(cond, bar) do { unsigned _sp = 0; while (cond) { __builtin_amdgcn_s_sleep(1); \
;     if ((++_sp & 255u) == 0u) { if (xb_ld(&(bar)[XB_TMO])) break; if (_sp > XB_SPIN_CAP) { atomicAdd(&(bar)[XB_TMO], 1u); break; } } } } while (0)
; __device__ __forceinline__ void xcd_barrier(const XcdBarrier& b) {
;     ...
;             if (og + 1u == (tg + 1u) * nx) xb_add(&bar[XB_TOPGEN], 1u);
;             else XB_SPIN(xb_ld(&bar[XB_TOPGEN]) == tg, bar);
;             __builtin_amdgcn_fence(__ATOMIC_ACQUIRE, "agent");
;             xb_add(&bar[XB_XGEN(b.x)], 1u);
;             asm volatile("s_waitcnt vmcnt(0)" ::: "memory");
.LBB0_1423:
	s_or_b64 exec, exec, s[20:21]
	s_and_saveexec_b64 s[20:21], s[36:37]
	s_cbranch_execz .LBB0_1425
.LBB0_1425:
	s_or_b64 exec, exec, s[20:21]
	s_waitcnt vmcnt(0)
	buffer_inv sc1
	s_waitcnt vmcnt(0)
.LBB0_1426:
	s_or_b64 exec, exec, s[2:3]
	s_waitcnt lgkmcnt(0)
	s_barrier

; __device__ __forceinline__ unsigned xb_ld(unsigned* p)              { return __hip_atomic_load(p, __ATOMIC_RELAXED, __HIP_MEMORY_SCOPE_AGENT); }
; __device__ __forceinline__ unsigned xb_add(unsigned* p, unsigned v) { return __hip_atomic_fetch_add(p, v, __ATOMIC_RELAXED, __HIP_MEMORY_SCOPE_AGENT); }
; #define XB_SPIN(cond, bar) do { unsigned _sp = 0; while (cond) { __builtin_amdgcn_s_sleep(1); \
;     if ((++_sp & 255u) == 0u) { if (xb_ld(&(bar)[XB_TMO])) break; if (_sp > XB_SPIN_CAP) { atomicAdd(&(bar)[XB_TMO], 1u); break; } } } } while (0)
; __device__ __forceinline__ void xcd_barrier(const XcdBarrier& b) {
;     ...
;         const unsigned old = xb_add(&bar[XB_XSUB(b.x)], 1u);
;         const unsigned gen = old / nloc;
;         if (old + 1u == (gen + 1u) * nloc) {
;             __builtin_amdgcn_fence(__ATOMIC_RELEASE, "agent");
;             asm volatile("s_waitcnt vmcnt(0)" ::: "memory");
;             const unsigned og = xb_add(&bar[XB_TOP], 1u);
;             const unsigned tg = og / nx;
;             if (og + 1u == (tg + 1u) * nx) xb_add(&bar[XB_TOPGEN], 1u);
;             else XB_SPIN(xb_ld(&bar[XB_TOPGEN]) == tg, bar);
;             __builtin_amdgcn_fence(__ATOMIC_ACQUIRE, "agent");
;             xb_add(&bar[XB_XGEN(b.x)], 1u);
;             asm volatile("s_waitcnt vmcnt(0)" ::: "memory");
;         } else {
;             XB_SPIN(xb_ld(&bar[XB_XGEN(b.x)]) == gen, bar);
.LBB0_1489:
	v_readlane_b32 s8, v254, 8
	v_readlane_b32 s9, v254, 9
	v_cvt_f32_u32_e32 v1, v2
	v_sub_u32_e32 v4, 0, v2
	v_rcp_iflag_f32_e32 v1, v1
	s_nop 1
	global_atomic_add v3, v193, v226, s[8:9] sc0
	v_mul_f32_e32 v1, 0x4f7ffffe, v1
	v_cvt_u32_f32_e32 v1, v1
	v_mul_lo_u32 v4, v4, v1
	v_mul_hi_u32 v4, v1, v4
	v_add_u32_e32 v1, v1, v4
	s_waitcnt vmcnt(0)
	v_mul_hi_u32 v1, v3, v1
	v_mul_lo_u32 v4, v1, v2
	v_sub_u32_e32 v4, v3, v4
	v_add_u32_e32 v5, 1, v1
	v_cmp_ge_u32_e32 vcc, v4, v2
	v_add_u32_e32 v3, 1, v3
	s_nop 0
	v_cndmask_b32_e32 v1, v1, v5, vcc
	v_sub_u32_e32 v5, v4, v2
	v_cndmask_b32_e32 v4, v4, v5, vcc
	v_add_u32_e32 v5, 1, v1
	v_cmp_ge_u32_e32 vcc, v4, v2
	s_nop 1
	v_cndmask_b32_e32 v1, v1, v5, vcc
	v_mul_lo_u32 v4, v2, v1
	v_add_u32_e32 v2, v4, v2
	v_cmp_ne_u32_e32 vcc, v3, v2
	s_and_saveexec_b64 s[18:19], vcc
	s_xor_b64 s[20:21], exec, s[18:19]
	s_cbranch_execz .LBB0_1503
	v_readlane_b32 s8, v254, 12
	v_readlane_b32 s9, v254, 13
	s_waitcnt lgkmcnt(0)
	v_add_u32_e32 v5, 1, v1
	v_mul_lo_u32 v5, v5, v0
	s_nop 3
	global_load_dword v0, v193, s[8:9] sc1
	s_waitcnt vmcnt(0)
	v_cmp_lt_u32_e32 vcc, v0, v5
	s_and_saveexec_b64 s[38:39], vcc
	s_cbranch_execz .LBB0_1502
	s_mov_b32 s5, 1
	s_mov_b64 s[40:41], 0
	s_branch .LBB0_1493

; __device__ __forceinline__ unsigned xb_ld(unsigned* p)              { return __hip_atomic_load(p, __ATOMIC_RELAXED, __HIP_MEMORY_SCOPE_AGENT); }
; __device__ __forceinline__ unsigned xb_add(unsigned* p, unsigned v) { return __hip_atomic_fetch_add(p, v, __ATOMIC_RELAXED, __HIP_MEMORY_SCOPE_AGENT); }
; #define XB_SPIN(cond, bar) do { unsigned _sp = 0; while (cond) { __builtin_amdgcn_s_sleep(1); \
;     if ((++_sp & 255u) == 0u) { if (xb_ld(&(bar)[XB_TMO])) break; if (_sp > XB_SPIN_CAP) { atomicAdd(&(bar)[XB_TMO], 1u); break; } } } } while (0)
; __device__ __forceinline__ void xcd_barrier(const XcdBarrier& b) {
;     ...
;             const unsigned og = xb_add(&bar[XB_TOP], 1u);
;             const unsigned tg = og / nx;
;             if (og + 1u == (tg + 1u) * nx) xb_add(&bar[XB_TOPGEN], 1u);
;             else XB_SPIN(xb_ld(&bar[XB_TOPGEN]) == tg, bar);
.LBB0_1506:
	s_or_b64 exec, exec, s[38:39]
	s_waitcnt vmcnt(0)
	v_readfirstlane_b32 s0, v2
	v_cvt_f32_u32_e32 v2, v0
	v_sub_u32_e32 v3, 0, v0
	v_add_u32_e32 v1, s0, v1
	v_readlane_b32 s8, v254, 14
	v_rcp_iflag_f32_e32 v2, v2
	v_readlane_b32 s9, v254, 15
	s_mov_b64 s[38:39], -1
	v_mul_f32_e32 v2, 0x4f7ffffe, v2
	v_cvt_u32_f32_e32 v2, v2
	v_mul_lo_u32 v3, v3, v2
	v_mul_hi_u32 v3, v2, v3
	v_add_u32_e32 v2, v2, v3
	v_mul_hi_u32 v2, v1, v2
	v_mul_lo_u32 v3, v2, v0
	v_sub_u32_e32 v3, v1, v3
	v_cmp_ge_u32_e32 vcc, v3, v0
	v_add_u32_e32 v4, 1, v2
	v_add_u32_e32 v1, 1, v1
	v_cndmask_b32_e32 v2, v2, v4, vcc
	v_sub_u32_e32 v4, v3, v0
	v_cndmask_b32_e32 v3, v3, v4, vcc
	v_cmp_ge_u32_e32 vcc, v3, v0
	v_add_u32_e32 v3, 1, v2
	s_nop 0
	v_cndmask_b32_e32 v2, v2, v3, vcc
	v_mul_lo_u32 v3, v0, v2
	v_add_u32_e32 v0, v3, v0
	v_cmp_ne_u32_e32 vcc, v1, v0
	v_mov_b32_e32 v5, v0
	v_mov_b64_e32 v[0:1], s[8:9]
	s_and_saveexec_b64 s[20:21], vcc
	s_cbranch_execz .LBB0_1518
	v_readlane_b32 s8, v254, 12
	v_readlane_b32 s9, v254, 13
	s_mov_b64 s[40:41], 0
	s_nop 3
	global_load_dword v0, v193, s[8:9] sc1
	s_waitcnt vmcnt(0)
	v_cmp_lt_u32_e32 vcc, v0, v5
	s_and_saveexec_b64 s[38:39], vcc
	s_cbranch_execz .LBB0_1517
	s_mov_b32 s5, 1
	s_branch .LBB0_1510

; __device__ __forceinline__ unsigned xb_ld(unsigned* p)              { return __hip_atomic_load(p, __ATOMIC_RELAXED, __HIP_MEMORY_SCOPE_AGENT); }
; __device__ __forceinline__ unsigned xb_add(unsigned* p, unsigned v) { return __hip_atomic_fetch_add(p, v, __ATOMIC_RELAXED, __HIP_MEMORY_SCOPE_AGENT); }
; #define XB_SPIN(cond, bar) do { unsigned _sp = 0; while (cond) { __builtin_amdgcn_s_sleep(1); \
;     if ((++_sp & 255u) == 0u) { if (xb_ld(&(bar)[XB_TMO])) break; if (_sp > XB_SPIN_CAP) { atomicAdd(&(bar)[XB_TMO], 1u); break; } } } } while (0)
; __device__ __forceinline__ void xcd_barrier(const XcdBarrier& b) {
;     ...
;             if (og + 1u == (tg + 1u) * nx) xb_add(&bar[XB_TOPGEN], 1u);
;             else XB_SPIN(xb_ld(&bar[XB_TOPGEN]) == tg, bar);
;             __builtin_amdgcn_fence(__ATOMIC_ACQUIRE, "agent");
;             xb_add(&bar[XB_XGEN(b.x)], 1u);
;             asm volatile("s_waitcnt vmcnt(0)" ::: "memory");
.LBB0_1518:
	s_or_b64 exec, exec, s[20:21]
	s_and_saveexec_b64 s[20:21], s[38:39]
	s_cbranch_execz .LBB0_1520
.LBB0_1520:
	s_or_b64 exec, exec, s[20:21]
	s_waitcnt vmcnt(0)
	buffer_inv sc1
	s_waitcnt vmcnt(0)
.LBB0_1521:
	s_or_b64 exec, exec, s[2:3]
	s_waitcnt lgkmcnt(0)
	s_barrier

; __device__ __forceinline__ unsigned xb_ld(unsigned* p)              { return __hip_atomic_load(p, __ATOMIC_RELAXED, __HIP_MEMORY_SCOPE_AGENT); }
; __device__ __forceinline__ unsigned xb_add(unsigned* p, unsigned v) { return __hip_atomic_fetch_add(p, v, __ATOMIC_RELAXED, __HIP_MEMORY_SCOPE_AGENT); }
; #define XB_SPIN(cond, bar) do { unsigned _sp = 0; while (cond) { __builtin_amdgcn_s_sleep(1); \
;     if ((++_sp & 255u) == 0u) { if (xb_ld(&(bar)[XB_TMO])) break; if (_sp > XB_SPIN_CAP) { atomicAdd(&(bar)[XB_TMO], 1u); break; } } } } while (0)
; __device__ __forceinline__ void xcd_barrier(const XcdBarrier& b) {
;     ...
;             if (og + 1u == (tg + 1u) * nx) xb_add(&bar[XB_TOPGEN], 1u);
;             else XB_SPIN(xb_ld(&bar[XB_TOPGEN]) == tg, bar);
;             __builtin_amdgcn_fence(__ATOMIC_ACQUIRE, "agent");
;             xb_add(&bar[XB_XGEN(b.x)], 1u);
;             asm volatile("s_waitcnt vmcnt(0)" ::: "memory");
.LBB0_1682:
	s_or_b64 exec, exec, s[20:21]
	s_and_saveexec_b64 s[20:21], s[36:37]
	s_cbranch_execz .LBB0_1684
.LBB0_1684:
	s_or_b64 exec, exec, s[20:21]
	s_waitcnt vmcnt(0)
	buffer_inv sc1
	s_waitcnt vmcnt(0)
.LBB0_1685:
	s_or_b64 exec, exec, s[2:3]
	s_waitcnt lgkmcnt(0)
	s_barrier

; __device__ __forceinline__ unsigned xb_ld(unsigned* p)              { return __hip_atomic_load(p, __ATOMIC_RELAXED, __HIP_MEMORY_SCOPE_AGENT); }
; __device__ __forceinline__ unsigned xb_add(unsigned* p, unsigned v) { return __hip_atomic_fetch_add(p, v, __ATOMIC_RELAXED, __HIP_MEMORY_SCOPE_AGENT); }
; #define XB_SPIN(cond, bar) do { unsigned _sp = 0; while (cond) { __builtin_amdgcn_s_sleep(1); \
;     if ((++_sp & 255u) == 0u) { if (xb_ld(&(bar)[XB_TMO])) break; if (_sp > XB_SPIN_CAP) { atomicAdd(&(bar)[XB_TMO], 1u); break; } } } } while (0)
; __device__ __forceinline__ void xcd_barrier(const XcdBarrier& b) {
;     ...
;         const unsigned old = xb_add(&bar[XB_XSUB(b.x)], 1u);
;         const unsigned gen = old / nloc;
;         if (old + 1u == (gen + 1u) * nloc) {
;             __builtin_amdgcn_fence(__ATOMIC_RELEASE, "agent");
;             asm volatile("s_waitcnt vmcnt(0)" ::: "memory");
;             const unsigned og = xb_add(&bar[XB_TOP], 1u);
;             const unsigned tg = og / nx;
;             if (og + 1u == (tg + 1u) * nx) xb_add(&bar[XB_TOPGEN], 1u);
;             else XB_SPIN(xb_ld(&bar[XB_TOPGEN]) == tg, bar);
;             __builtin_amdgcn_fence(__ATOMIC_ACQUIRE, "agent");
;             xb_add(&bar[XB_XGEN(b.x)], 1u);
;             asm volatile("s_waitcnt vmcnt(0)" ::: "memory");
;         } else {
;             XB_SPIN(xb_ld(&bar[XB_XGEN(b.x)]) == gen, bar);
.LBB0_1713:
	v_readlane_b32 s4, v254, 8
	v_readlane_b32 s5, v254, 9
	v_cvt_f32_u32_e32 v1, v2
	v_sub_u32_e32 v4, 0, v2
	v_rcp_iflag_f32_e32 v1, v1
	s_nop 1
	global_atomic_add v3, v193, v226, s[4:5] sc0
	v_mul_f32_e32 v1, 0x4f7ffffe, v1
	v_cvt_u32_f32_e32 v1, v1
	v_mul_lo_u32 v4, v4, v1
	v_mul_hi_u32 v4, v1, v4
	v_add_u32_e32 v1, v1, v4
	s_waitcnt vmcnt(0)
	v_mul_hi_u32 v1, v3, v1
	v_mul_lo_u32 v4, v1, v2
	v_sub_u32_e32 v4, v3, v4
	v_add_u32_e32 v5, 1, v1
	v_cmp_ge_u32_e32 vcc, v4, v2
	v_add_u32_e32 v3, 1, v3
	s_nop 0
	v_cndmask_b32_e32 v1, v1, v5, vcc
	v_sub_u32_e32 v5, v4, v2
	v_cndmask_b32_e32 v4, v4, v5, vcc
	v_add_u32_e32 v5, 1, v1
	v_cmp_ge_u32_e32 vcc, v4, v2
	s_nop 1
	v_cndmask_b32_e32 v1, v1, v5, vcc
	v_mul_lo_u32 v4, v2, v1
	v_add_u32_e32 v2, v4, v2
	v_cmp_ne_u32_e32 vcc, v3, v2
	s_and_saveexec_b64 s[4:5], vcc
	s_xor_b64 s[18:19], exec, s[4:5]
	s_cbranch_execz .LBB0_1727
	v_readlane_b32 s4, v254, 12
	v_readlane_b32 s5, v254, 13
	s_waitcnt lgkmcnt(0)
	v_add_u32_e32 v5, 1, v1
	v_mul_lo_u32 v5, v5, v0
	s_nop 3
	global_load_dword v0, v193, s[4:5] sc1
	s_waitcnt vmcnt(0)
	v_cmp_lt_u32_e32 vcc, v0, v5
	s_and_saveexec_b64 s[20:21], vcc
	s_cbranch_execz .LBB0_1726
	s_mov_b32 s4, 1
	s_mov_b64 s[36:37], 0
	s_branch .LBB0_1717

; __device__ __forceinline__ unsigned xb_ld(unsigned* p)              { return __hip_atomic_load(p, __ATOMIC_RELAXED, __HIP_MEMORY_SCOPE_AGENT); }
; #define XB_SPIN(cond, bar) do { unsigned _sp = 0; while (cond) { __builtin_amdgcn_s_sleep(1); \
;     if ((++_sp & 255u) == 0u) { if (xb_ld(&(bar)[XB_TMO])) break; if (_sp > XB_SPIN_CAP) { atomicAdd(&(bar)[XB_TMO], 1u); break; } } } } while (0)
; __device__ __forceinline__ void xcd_barrier(const XcdBarrier& b) {
;     ...
;             XB_SPIN(xb_ld(&bar[XB_XGEN(b.x)]) == gen, bar);
.LBB0_1721:
	v_readlane_b32 s8, v254, 12
	v_readlane_b32 s9, v254, 13
	s_add_i32 s4, s4, 1
	s_mov_b64 s[42:43], -1
	s_nop 2
	global_load_dword v0, v193, s[8:9] sc1
	s_waitcnt vmcnt(0)
	v_cmp_ge_u32_e32 vcc, v0, v5
	s_orn2_b64 s[40:41], vcc, exec
	s_branch .LBB0_1716

; __device__ __forceinline__ unsigned xb_ld(unsigned* p)              { return __hip_atomic_load(p, __ATOMIC_RELAXED, __HIP_MEMORY_SCOPE_AGENT); }
; __device__ __forceinline__ unsigned xb_add(unsigned* p, unsigned v) { return __hip_atomic_fetch_add(p, v, __ATOMIC_RELAXED, __HIP_MEMORY_SCOPE_AGENT); }
; #define XB_SPIN(cond, bar) do { unsigned _sp = 0; while (cond) { __builtin_amdgcn_s_sleep(1); \
;     if ((++_sp & 255u) == 0u) { if (xb_ld(&(bar)[XB_TMO])) break; if (_sp > XB_SPIN_CAP) { atomicAdd(&(bar)[XB_TMO], 1u); break; } } } } while (0)
; __device__ __forceinline__ void xcd_barrier(const XcdBarrier& b) {
;     ...
;             const unsigned og = xb_add(&bar[XB_TOP], 1u);
;             const unsigned tg = og / nx;
;             if (og + 1u == (tg + 1u) * nx) xb_add(&bar[XB_TOPGEN], 1u);
;             else XB_SPIN(xb_ld(&bar[XB_TOPGEN]) == tg, bar);
.LBB0_1730:
	s_or_b64 exec, exec, s[20:21]
	s_waitcnt vmcnt(0)
	v_readfirstlane_b32 s0, v2
	v_cvt_f32_u32_e32 v2, v0
	v_sub_u32_e32 v3, 0, v0
	v_add_u32_e32 v1, s0, v1
	v_readlane_b32 s4, v254, 14
	v_rcp_iflag_f32_e32 v2, v2
	v_readlane_b32 s5, v254, 15
	s_mov_b64 s[20:21], -1
	v_mul_f32_e32 v2, 0x4f7ffffe, v2
	v_cvt_u32_f32_e32 v2, v2
	v_mul_lo_u32 v3, v3, v2
	v_mul_hi_u32 v3, v2, v3
	v_add_u32_e32 v2, v2, v3
	v_mul_hi_u32 v2, v1, v2
	v_mul_lo_u32 v3, v2, v0
	v_sub_u32_e32 v3, v1, v3
	v_cmp_ge_u32_e32 vcc, v3, v0
	v_add_u32_e32 v4, 1, v2
	v_add_u32_e32 v1, 1, v1
	v_cndmask_b32_e32 v2, v2, v4, vcc
	v_sub_u32_e32 v4, v3, v0
	v_cndmask_b32_e32 v3, v3, v4, vcc
	v_cmp_ge_u32_e32 vcc, v3, v0
	v_add_u32_e32 v3, 1, v2
	s_nop 0
	v_cndmask_b32_e32 v2, v2, v3, vcc
	v_mul_lo_u32 v3, v0, v2
	v_add_u32_e32 v0, v3, v0
	v_cmp_ne_u32_e32 vcc, v1, v0
	v_mov_b32_e32 v5, v0
	v_mov_b64_e32 v[0:1], s[4:5]
	s_and_saveexec_b64 s[18:19], vcc
	s_cbranch_execz .LBB0_1742
	v_readlane_b32 s4, v254, 12
	v_readlane_b32 s5, v254, 13
	s_mov_b64 s[36:37], 0
	s_nop 3
	global_load_dword v0, v193, s[4:5] sc1
	s_waitcnt vmcnt(0)
	v_cmp_lt_u32_e32 vcc, v0, v5
	s_and_saveexec_b64 s[20:21], vcc
	s_cbranch_execz .LBB0_1741
	s_mov_b32 s4, 1
	s_branch .LBB0_1734

; __device__ __forceinline__ unsigned xb_add(unsigned* p, unsigned v) { return __hip_atomic_fetch_add(p, v, __ATOMIC_RELAXED, __HIP_MEMORY_SCOPE_AGENT); }
; __device__ __forceinline__ void xcd_barrier(const XcdBarrier& b) {
;     ...
;             if (og + 1u == (tg + 1u) * nx) xb_add(&bar[XB_TOPGEN], 1u);
.LBB0_1743:
	s_getpc_b64 s[98:99]
